# P11/P14 first-iteration peel too; P23: first K-iteration waits of units after the first allow the previous unit's 8 epilogue stores outstanding
# speedup vs baseline: 1.0054x; 1.0017x over previous
.LBB0_2935:
	s_andn2_b64 vcc, exec, s[14:15]
	s_cbranch_vccnz .Lzs_12
	s_add_i32 s28, s82, 0x80
	s_add_i32 s82, s83, 0x100
	s_mov_b32 s83, 0
	s_cmp_lg_u32 s99, 0
	s_cbranch_scc1 .Lrx23_first
	ds_read_b128 v[18:21], v180
	ds_read_b128 v[22:25], v181
	ds_read_b128 v[26:29], v188
	ds_read_b128 v[30:33], v189
	ds_read_b128 v[2:5], v182
	ds_read_b128 v[6:9], v183
	ds_read_b128 v[10:13], v190
	ds_read_b128 v[14:17], v191
	s_add_i32 s84, s28, 0x80
	s_cmp_eq_u32 s67, s83
	s_cselect_b32 s86, s25, s84
	s_cselect_b32 s87, s29, s82
	s_add_i32 s84, s86, 0x80
	s_add_i32 s85, s87, 0x80
	v_mov_b32_e32 v172, v176
	ds_read_b128 v[164:167], v196
	ds_read_b128 v[168:171], v196 offset:1024
	ds_read_b128 v[198:201], v196 offset:2048
	ds_read_b128 v[202:205], v196 offset:3072
	ds_read_b128 v[214:217], v196 offset:4096
	ds_read_b128 v[218:221], v196 offset:5120
	ds_read_b128 v[222:225], v196 offset:6144
	ds_read_b128 v[226:229], v196 offset:7168
	s_add_i32 s88, s28, s65
	v_add_u32_e32 v172, s88, v172
	s_add_i32 m0, s49, 0xc000
	s_add_i32 s88, s28, s70
	global_load_lds_dwordx4 v172, s[4:5]
	v_mov_b32_e32 v172, v176
	s_add_i32 m0, s49, 0xe000
	v_add_u32_e32 v172, s88, v172
	global_load_lds_dwordx4 v172, s[4:5]
	s_waitcnt vmcnt(8)
	s_waitcnt lgkmcnt(0)
	s_barrier
	s_setprio 1
	s_waitcnt lgkmcnt(0)
	v_mfma_f32_16x16x128_f8f6f4 v[158:161], v[18:25], v[164:171], 0
	v_mfma_f32_16x16x128_f8f6f4 v[154:157], v[26:33], v[164:171], 0
	v_mfma_f32_16x16x128_f8f6f4 v[150:153], v[18:25], v[198:205], 0
	v_mfma_f32_16x16x128_f8f6f4 v[146:149], v[26:33], v[198:205], 0
	v_mfma_f32_16x16x128_f8f6f4 v[138:141], v[18:25], v[214:221], 0
	v_mfma_f32_16x16x128_f8f6f4 v[130:133], v[26:33], v[214:221], 0
	v_mfma_f32_16x16x128_f8f6f4 v[122:125], v[18:25], v[222:229], 0
	v_mfma_f32_16x16x128_f8f6f4 v[114:117], v[26:33], v[222:229], 0
	s_setprio 0
	s_setprio 1
	v_mfma_f32_16x16x128_f8f6f4 v[142:145], v[2:9], v[164:171], 0
	v_mfma_f32_16x16x128_f8f6f4 v[134:137], v[10:17], v[164:171], 0
	v_mfma_f32_16x16x128_f8f6f4 v[126:129], v[2:9], v[198:205], 0
	v_mfma_f32_16x16x128_f8f6f4 v[118:121], v[10:17], v[198:205], 0
	v_mfma_f32_16x16x128_f8f6f4 v[110:113], v[2:9], v[214:221], 0
	v_mfma_f32_16x16x128_f8f6f4 v[106:109], v[10:17], v[214:221], 0
	v_mfma_f32_16x16x128_f8f6f4 v[102:105], v[2:9], v[222:229], 0
	v_mfma_f32_16x16x128_f8f6f4 v[98:101], v[10:17], v[222:229], 0
	s_setprio 0
	s_barrier
	v_mov_b32_e32 v172, v177
	ds_read_b128 v[164:167], v196 offset:16384
	ds_read_b128 v[168:171], v196 offset:17408
	ds_read_b128 v[198:201], v196 offset:18432
	ds_read_b128 v[202:205], v196 offset:19456
	ds_read_b128 v[214:217], v196 offset:20480
	ds_read_b128 v[218:221], v196 offset:21504
	ds_read_b128 v[222:225], v196 offset:22528
	ds_read_b128 v[226:229], v196 offset:23552
	s_mov_b32 m0, s50
	v_add_u32_e32 v172, s87, v172
	global_load_lds_dwordx4 v172, s[6:7]
	v_mov_b32_e32 v172, v177
	s_add_i32 s87, s87, s48
	v_add_u32_e32 v172, s87, v172
	s_mov_b32 m0, s51
	s_add_i32 s87, s87, s48
	global_load_lds_dwordx4 v172, s[6:7]
	v_mov_b32_e32 v172, v177
	s_mov_b32 m0, s52
	v_add_u32_e32 v172, s87, v172
	global_load_lds_dwordx4 v172, s[6:7]
	v_mov_b32_e32 v172, v177
	s_add_i32 s87, s87, s48
	v_add_u32_e32 v172, s87, v172
	s_mov_b32 m0, s53
	s_nop 0
	global_load_lds_dwordx4 v172, s[6:7]
	v_mov_b32_e32 v172, v176
	s_mov_b32 m0, s49
	v_add_u32_e32 v172, s86, v172
	global_load_lds_dwordx4 v172, s[4:5]
	v_mov_b32_e32 v172, v176
	s_add_i32 s86, s86, s47
	v_add_u32_e32 v172, s86, v172
	s_mov_b32 m0, s54
	s_nop 0
	global_load_lds_dwordx4 v172, s[4:5]
	s_waitcnt vmcnt(8)
	s_waitcnt lgkmcnt(0)
	s_barrier
	s_setprio 1
	s_waitcnt lgkmcnt(0)
	v_mfma_f32_16x16x128_f8f6f4 v[94:97], v[18:25], v[164:171], 0
	v_mfma_f32_16x16x128_f8f6f4 v[90:93], v[26:33], v[164:171], 0
	v_mfma_f32_16x16x128_f8f6f4 v[86:89], v[18:25], v[198:205], 0
	v_mfma_f32_16x16x128_f8f6f4 v[82:85], v[26:33], v[198:205], 0
	v_mfma_f32_16x16x128_f8f6f4 v[74:77], v[18:25], v[214:221], 0
	v_mfma_f32_16x16x128_f8f6f4 v[66:69], v[26:33], v[214:221], 0
	v_mfma_f32_16x16x128_f8f6f4 v[58:61], v[18:25], v[222:229], 0
	v_mfma_f32_16x16x128_f8f6f4 v[50:53], v[26:33], v[222:229], 0
	s_setprio 0
	s_setprio 1
	v_mfma_f32_16x16x128_f8f6f4 v[78:81], v[2:9], v[164:171], 0
	v_mfma_f32_16x16x128_f8f6f4 v[70:73], v[10:17], v[164:171], 0
	v_mfma_f32_16x16x128_f8f6f4 v[62:65], v[2:9], v[198:205], 0
	v_mfma_f32_16x16x128_f8f6f4 v[54:57], v[10:17], v[198:205], 0
	v_mfma_f32_16x16x128_f8f6f4 v[46:49], v[2:9], v[214:221], 0
	v_mfma_f32_16x16x128_f8f6f4 v[42:45], v[10:17], v[214:221], 0
	v_mfma_f32_16x16x128_f8f6f4 v[38:41], v[2:9], v[222:229], 0
	v_mfma_f32_16x16x128_f8f6f4 v[34:37], v[10:17], v[222:229], 0
	s_setprio 0
	s_barrier
	s_branch .Lmid_10
.Lrx23_first:
	ds_read_b128 v[18:21], v180
	ds_read_b128 v[22:25], v181
	ds_read_b128 v[26:29], v188
	ds_read_b128 v[30:33], v189
	ds_read_b128 v[2:5], v182
	ds_read_b128 v[6:9], v183
	ds_read_b128 v[10:13], v190
	ds_read_b128 v[14:17], v191
	s_add_i32 s84, s28, 0x80
	s_cmp_eq_u32 s67, s83
	s_cselect_b32 s86, s25, s84
	s_cselect_b32 s87, s29, s82
	s_add_i32 s84, s86, 0x80
	s_add_i32 s85, s87, 0x80
	v_mov_b32_e32 v172, v176
	ds_read_b128 v[164:167], v196
	ds_read_b128 v[168:171], v196 offset:1024
	ds_read_b128 v[198:201], v196 offset:2048
	ds_read_b128 v[202:205], v196 offset:3072
	ds_read_b128 v[214:217], v196 offset:4096
	ds_read_b128 v[218:221], v196 offset:5120
	ds_read_b128 v[222:225], v196 offset:6144
	ds_read_b128 v[226:229], v196 offset:7168
	s_add_i32 s88, s28, s65
	v_add_u32_e32 v172, s88, v172
	s_add_i32 m0, s49, 0xc000
	s_add_i32 s88, s28, s70
	global_load_lds_dwordx4 v172, s[4:5]
	v_mov_b32_e32 v172, v176
	s_add_i32 m0, s49, 0xe000
	v_add_u32_e32 v172, s88, v172
	global_load_lds_dwordx4 v172, s[4:5]
	s_waitcnt vmcnt(16)
	s_waitcnt lgkmcnt(0)
	s_barrier
	s_setprio 1
	s_waitcnt lgkmcnt(0)
	v_mfma_f32_16x16x128_f8f6f4 v[158:161], v[18:25], v[164:171], 0
	v_mfma_f32_16x16x128_f8f6f4 v[154:157], v[26:33], v[164:171], 0
	v_mfma_f32_16x16x128_f8f6f4 v[150:153], v[18:25], v[198:205], 0
	v_mfma_f32_16x16x128_f8f6f4 v[146:149], v[26:33], v[198:205], 0
	v_mfma_f32_16x16x128_f8f6f4 v[138:141], v[18:25], v[214:221], 0
	v_mfma_f32_16x16x128_f8f6f4 v[130:133], v[26:33], v[214:221], 0
	v_mfma_f32_16x16x128_f8f6f4 v[122:125], v[18:25], v[222:229], 0
	v_mfma_f32_16x16x128_f8f6f4 v[114:117], v[26:33], v[222:229], 0
	s_setprio 0
	s_setprio 1
	v_mfma_f32_16x16x128_f8f6f4 v[142:145], v[2:9], v[164:171], 0
	v_mfma_f32_16x16x128_f8f6f4 v[134:137], v[10:17], v[164:171], 0
	v_mfma_f32_16x16x128_f8f6f4 v[126:129], v[2:9], v[198:205], 0
	v_mfma_f32_16x16x128_f8f6f4 v[118:121], v[10:17], v[198:205], 0
	v_mfma_f32_16x16x128_f8f6f4 v[110:113], v[2:9], v[214:221], 0
	v_mfma_f32_16x16x128_f8f6f4 v[106:109], v[10:17], v[214:221], 0
	v_mfma_f32_16x16x128_f8f6f4 v[102:105], v[2:9], v[222:229], 0
	v_mfma_f32_16x16x128_f8f6f4 v[98:101], v[10:17], v[222:229], 0
	s_setprio 0
	s_barrier
	v_mov_b32_e32 v172, v177
	ds_read_b128 v[164:167], v196 offset:16384
	ds_read_b128 v[168:171], v196 offset:17408
	ds_read_b128 v[198:201], v196 offset:18432
	ds_read_b128 v[202:205], v196 offset:19456
	ds_read_b128 v[214:217], v196 offset:20480
	ds_read_b128 v[218:221], v196 offset:21504
	ds_read_b128 v[222:225], v196 offset:22528
	ds_read_b128 v[226:229], v196 offset:23552
	s_mov_b32 m0, s50
	v_add_u32_e32 v172, s87, v172
	global_load_lds_dwordx4 v172, s[6:7]
	v_mov_b32_e32 v172, v177
	s_add_i32 s87, s87, s48
	v_add_u32_e32 v172, s87, v172
	s_mov_b32 m0, s51
	s_add_i32 s87, s87, s48
	global_load_lds_dwordx4 v172, s[6:7]
	v_mov_b32_e32 v172, v177
	s_mov_b32 m0, s52
	v_add_u32_e32 v172, s87, v172
	global_load_lds_dwordx4 v172, s[6:7]
	v_mov_b32_e32 v172, v177
	s_add_i32 s87, s87, s48
	v_add_u32_e32 v172, s87, v172
	s_mov_b32 m0, s53
	s_nop 0
	global_load_lds_dwordx4 v172, s[6:7]
	v_mov_b32_e32 v172, v176
	s_mov_b32 m0, s49
	v_add_u32_e32 v172, s86, v172
	global_load_lds_dwordx4 v172, s[4:5]
	v_mov_b32_e32 v172, v176
	s_add_i32 s86, s86, s47
	v_add_u32_e32 v172, s86, v172
	s_mov_b32 m0, s54
	s_nop 0
	global_load_lds_dwordx4 v172, s[4:5]
	s_waitcnt vmcnt(16)
	s_waitcnt lgkmcnt(0)
	s_barrier
	s_setprio 1
	s_waitcnt lgkmcnt(0)
	v_mfma_f32_16x16x128_f8f6f4 v[94:97], v[18:25], v[164:171], 0
	v_mfma_f32_16x16x128_f8f6f4 v[90:93], v[26:33], v[164:171], 0
	v_mfma_f32_16x16x128_f8f6f4 v[86:89], v[18:25], v[198:205], 0
	v_mfma_f32_16x16x128_f8f6f4 v[82:85], v[26:33], v[198:205], 0
	v_mfma_f32_16x16x128_f8f6f4 v[74:77], v[18:25], v[214:221], 0
	v_mfma_f32_16x16x128_f8f6f4 v[66:69], v[26:33], v[214:221], 0
	v_mfma_f32_16x16x128_f8f6f4 v[58:61], v[18:25], v[222:229], 0
	v_mfma_f32_16x16x128_f8f6f4 v[50:53], v[26:33], v[222:229], 0
	s_setprio 0
	s_setprio 1
	v_mfma_f32_16x16x128_f8f6f4 v[78:81], v[2:9], v[164:171], 0
	v_mfma_f32_16x16x128_f8f6f4 v[70:73], v[10:17], v[164:171], 0
	v_mfma_f32_16x16x128_f8f6f4 v[62:65], v[2:9], v[198:205], 0
	v_mfma_f32_16x16x128_f8f6f4 v[54:57], v[10:17], v[198:205], 0
	v_mfma_f32_16x16x128_f8f6f4 v[46:49], v[2:9], v[214:221], 0
	v_mfma_f32_16x16x128_f8f6f4 v[42:45], v[10:17], v[214:221], 0
	v_mfma_f32_16x16x128_f8f6f4 v[38:41], v[2:9], v[222:229], 0
	v_mfma_f32_16x16x128_f8f6f4 v[34:37], v[10:17], v[222:229], 0
	s_setprio 0
	s_barrier
	s_branch .Lmid_10

.Ltx23_skip:
.Lmid_10:
	ds_read_b128 v[2:5], v184
	ds_read_b128 v[6:9], v185
	ds_read_b128 v[10:13], v192
	ds_read_b128 v[14:17], v193
	ds_read_b128 v[18:21], v186
	ds_read_b128 v[22:25], v187
	ds_read_b128 v[26:29], v194
	ds_read_b128 v[30:33], v195
	v_mov_b32_e32 v172, v176
	ds_read_b128 v[164:167], v196 offset:32768
	ds_read_b128 v[168:171], v196 offset:33792
	ds_read_b128 v[198:201], v196 offset:34816
	ds_read_b128 v[202:205], v196 offset:35840
	ds_read_b128 v[214:217], v196 offset:36864
	ds_read_b128 v[218:221], v196 offset:37888
	ds_read_b128 v[222:225], v196 offset:38912
	ds_read_b128 v[226:229], v196 offset:39936
	s_add_i32 s86, s86, s47
	s_mov_b32 m0, s55
	v_add_u32_e32 v172, s86, v172
	global_load_lds_dwordx4 v172, s[4:5]
	v_mov_b32_e32 v172, v176
	s_add_i32 s86, s86, s47
	v_add_u32_e32 v172, s86, v172
	s_mov_b32 m0, s56
	s_nop 0
	global_load_lds_dwordx4 v172, s[4:5]
	s_waitcnt vmcnt(8)
	s_waitcnt lgkmcnt(0)
	s_barrier
	s_setprio 1
	s_waitcnt lgkmcnt(0)
	v_mfma_f32_16x16x128_f8f6f4 v[158:161], v[2:9], v[164:171], v[158:161]
	v_mfma_f32_16x16x128_f8f6f4 v[154:157], v[10:17], v[164:171], v[154:157]
	v_mfma_f32_16x16x128_f8f6f4 v[150:153], v[2:9], v[198:205], v[150:153]
	v_mfma_f32_16x16x128_f8f6f4 v[146:149], v[10:17], v[198:205], v[146:149]
	v_mfma_f32_16x16x128_f8f6f4 v[138:141], v[2:9], v[214:221], v[138:141]
	v_mfma_f32_16x16x128_f8f6f4 v[130:133], v[10:17], v[214:221], v[130:133]
	v_mfma_f32_16x16x128_f8f6f4 v[122:125], v[2:9], v[222:229], v[122:125]
	v_mfma_f32_16x16x128_f8f6f4 v[114:117], v[10:17], v[222:229], v[114:117]
	s_setprio 0
	s_setprio 1
	v_mfma_f32_16x16x128_f8f6f4 v[142:145], v[18:25], v[164:171], v[142:145]
	v_mfma_f32_16x16x128_f8f6f4 v[134:137], v[26:33], v[164:171], v[134:137]
	v_mfma_f32_16x16x128_f8f6f4 v[126:129], v[18:25], v[198:205], v[126:129]
	v_mfma_f32_16x16x128_f8f6f4 v[118:121], v[26:33], v[198:205], v[118:121]
	v_mfma_f32_16x16x128_f8f6f4 v[110:113], v[18:25], v[214:221], v[110:113]
	v_mfma_f32_16x16x128_f8f6f4 v[106:109], v[26:33], v[214:221], v[106:109]
	v_mfma_f32_16x16x128_f8f6f4 v[102:105], v[18:25], v[222:229], v[102:105]
	v_mfma_f32_16x16x128_f8f6f4 v[98:101], v[26:33], v[222:229], v[98:101]
	s_setprio 0
	s_barrier
	s_cmp_eq_u32 s67, s83
	s_cbranch_scc1 .Lh23_last
	v_mov_b32_e32 v172, v177
	ds_read_b128 v[164:167], v196 offset:49152
	ds_read_b128 v[168:171], v196 offset:50176
	ds_read_b128 v[198:201], v196 offset:51200
	ds_read_b128 v[202:205], v196 offset:52224
	ds_read_b128 v[214:217], v196 offset:53248
	ds_read_b128 v[218:221], v196 offset:54272
	ds_read_b128 v[222:225], v196 offset:55296
	ds_read_b128 v[226:229], v196 offset:56320
	s_mov_b32 m0, s58
	v_add_u32_e32 v172, s85, v172
	global_load_lds_dwordx4 v172, s[6:7]
	v_mov_b32_e32 v172, v177
	s_add_i32 s85, s85, s48
	v_add_u32_e32 v172, s85, v172
	s_mov_b32 m0, s59
	s_add_i32 s85, s85, s48
	global_load_lds_dwordx4 v172, s[6:7]
	v_mov_b32_e32 v172, v177
	s_mov_b32 m0, s62
	v_add_u32_e32 v172, s85, v172
	global_load_lds_dwordx4 v172, s[6:7]
	v_mov_b32_e32 v172, v177
	s_add_i32 s85, s85, s48
	v_add_u32_e32 v172, s85, v172
	s_mov_b32 m0, s63
	s_nop 0
	global_load_lds_dwordx4 v172, s[6:7]
	v_mov_b32_e32 v172, v176
	s_mov_b32 m0, s60
	v_add_u32_e32 v172, s84, v172
	global_load_lds_dwordx4 v172, s[4:5]
	v_mov_b32_e32 v172, v176
	s_add_i32 s84, s84, s47
	v_add_u32_e32 v172, s84, v172
	s_mov_b32 m0, s61
	s_nop 0
	global_load_lds_dwordx4 v172, s[4:5]
	s_waitcnt vmcnt(8)
	s_waitcnt lgkmcnt(0)
	s_barrier
	s_setprio 1
	s_waitcnt lgkmcnt(0)
	v_mfma_f32_16x16x128_f8f6f4 v[94:97], v[2:9], v[164:171], v[94:97]
	v_mfma_f32_16x16x128_f8f6f4 v[90:93], v[10:17], v[164:171], v[90:93]
	v_mfma_f32_16x16x128_f8f6f4 v[86:89], v[2:9], v[198:205], v[86:89]
	v_mfma_f32_16x16x128_f8f6f4 v[82:85], v[10:17], v[198:205], v[82:85]
	v_mfma_f32_16x16x128_f8f6f4 v[74:77], v[2:9], v[214:221], v[74:77]
	v_mfma_f32_16x16x128_f8f6f4 v[66:69], v[10:17], v[214:221], v[66:69]
	v_mfma_f32_16x16x128_f8f6f4 v[58:61], v[2:9], v[222:229], v[58:61]
	v_mfma_f32_16x16x128_f8f6f4 v[50:53], v[10:17], v[222:229], v[50:53]
	s_setprio 0
	s_setprio 1
	v_mfma_f32_16x16x128_f8f6f4 v[78:81], v[18:25], v[164:171], v[78:81]
	v_mfma_f32_16x16x128_f8f6f4 v[70:73], v[26:33], v[164:171], v[70:73]
	v_mfma_f32_16x16x128_f8f6f4 v[62:65], v[18:25], v[198:205], v[62:65]
	v_mfma_f32_16x16x128_f8f6f4 v[54:57], v[26:33], v[198:205], v[54:57]
	v_mfma_f32_16x16x128_f8f6f4 v[46:49], v[18:25], v[214:221], v[46:49]
	v_mfma_f32_16x16x128_f8f6f4 v[42:45], v[26:33], v[214:221], v[42:45]
	v_mfma_f32_16x16x128_f8f6f4 v[38:41], v[18:25], v[222:229], v[38:41]
	v_mfma_f32_16x16x128_f8f6f4 v[34:37], v[26:33], v[222:229], v[34:37]
	s_setprio 0
	s_barrier
	s_add_i32 s83, s83, 2
	s_addk_i32 s28, 0x100
	s_addk_i32 s82, 0x100
	s_cmp_ge_i32 s83, s64
	s_cbranch_scc0 .LBB0_2937
	s_branch .LBB0_2939

.Lh23_epi1:
	v_pk_fma_f32 v[94:95], v[94:95], s[18:19], 0 op_sel_hi:[1,0,0]
	v_pk_fma_f32 v[96:97], v[96:97], s[18:19], 0 op_sel_hi:[1,0,0]
	v_pk_fma_f32 v[90:91], v[90:91], s[18:19], 0 op_sel_hi:[1,0,0]
	v_pk_fma_f32 v[92:93], v[92:93], s[18:19], 0 op_sel_hi:[1,0,0]
	v_pk_fma_f32 v[78:79], v[78:79], s[20:21], 0 op_sel_hi:[1,0,0]
	v_pk_fma_f32 v[80:81], v[80:81], s[20:21], 0 op_sel_hi:[1,0,0]
	v_pk_fma_f32 v[70:71], v[70:71], s[20:21], 0 op_sel_hi:[1,0,0]
	v_pk_fma_f32 v[72:73], v[72:73], s[20:21], 0 op_sel_hi:[1,0,0]
	v_pk_fma_f32 v[86:87], v[86:87], s[18:19], 0 op_sel_hi:[1,0,0]
	v_pk_fma_f32 v[88:89], v[88:89], s[18:19], 0 op_sel_hi:[1,0,0]
	v_pk_fma_f32 v[82:83], v[82:83], s[18:19], 0 op_sel_hi:[1,0,0]
	v_pk_fma_f32 v[84:85], v[84:85], s[18:19], 0 op_sel_hi:[1,0,0]
	v_pk_fma_f32 v[62:63], v[62:63], s[20:21], 0 op_sel_hi:[1,0,0]
	v_pk_fma_f32 v[64:65], v[64:65], s[20:21], 0 op_sel_hi:[1,0,0]
	v_pk_fma_f32 v[54:55], v[54:55], s[20:21], 0 op_sel_hi:[1,0,0]
	v_pk_fma_f32 v[56:57], v[56:57], s[20:21], 0 op_sel_hi:[1,0,0]
	v_pk_mul_f32 v[230:231], v[94:95], s[98:99] op_sel_hi:[1,0]
	v_pk_mul_f32 v[232:233], v[96:97], s[98:99] op_sel_hi:[1,0]
	v_pk_mul_f32 v[234:235], v[90:91], s[98:99] op_sel_hi:[1,0]
	v_pk_mul_f32 v[236:237], v[92:93], s[98:99] op_sel_hi:[1,0]
	v_pk_mul_f32 v[238:239], v[86:87], s[98:99] op_sel_hi:[1,0]
	v_pk_mul_f32 v[240:241], v[88:89], s[98:99] op_sel_hi:[1,0]
	v_pk_mul_f32 v[242:243], v[82:83], s[98:99] op_sel_hi:[1,0]
	v_pk_mul_f32 v[244:245], v[84:85], s[98:99] op_sel_hi:[1,0]
	v_exp_f32_e32 v230, v230
	v_exp_f32_e32 v231, v231
	v_exp_f32_e32 v232, v232
	v_exp_f32_e32 v233, v233
	v_exp_f32_e32 v234, v234
	v_exp_f32_e32 v235, v235
	v_exp_f32_e32 v236, v236
	v_exp_f32_e32 v237, v237
	v_exp_f32_e32 v238, v238
	v_exp_f32_e32 v239, v239
	v_exp_f32_e32 v240, v240
	v_exp_f32_e32 v241, v241
	v_exp_f32_e32 v242, v242
	v_exp_f32_e32 v243, v243
	v_exp_f32_e32 v244, v244
	v_exp_f32_e32 v245, v245
	v_pk_add_f32 v[230:231], v[230:231], 1.0 op_sel_hi:[1,0]
	v_pk_add_f32 v[232:233], v[232:233], 1.0 op_sel_hi:[1,0]
	v_pk_add_f32 v[234:235], v[234:235], 1.0 op_sel_hi:[1,0]
	v_pk_add_f32 v[236:237], v[236:237], 1.0 op_sel_hi:[1,0]
	v_pk_add_f32 v[238:239], v[238:239], 1.0 op_sel_hi:[1,0]
	v_pk_add_f32 v[240:241], v[240:241], 1.0 op_sel_hi:[1,0]
	v_pk_add_f32 v[242:243], v[242:243], 1.0 op_sel_hi:[1,0]
	v_pk_add_f32 v[244:245], v[244:245], 1.0 op_sel_hi:[1,0]
	v_rcp_f32_e32 v230, v230
	v_rcp_f32_e32 v231, v231
	v_rcp_f32_e32 v232, v232
	v_rcp_f32_e32 v233, v233
	v_rcp_f32_e32 v234, v234
	v_rcp_f32_e32 v235, v235
	v_rcp_f32_e32 v236, v236
	v_rcp_f32_e32 v237, v237
	v_rcp_f32_e32 v238, v238
	v_rcp_f32_e32 v239, v239
	v_rcp_f32_e32 v240, v240
	v_rcp_f32_e32 v241, v241
	v_rcp_f32_e32 v242, v242
	v_rcp_f32_e32 v243, v243
	v_rcp_f32_e32 v244, v244
	v_rcp_f32_e32 v245, v245
	v_pk_mul_f32 v[230:231], v[94:95], v[230:231]
	v_pk_mul_f32 v[232:233], v[96:97], v[232:233]
	v_pk_mul_f32 v[234:235], v[90:91], v[234:235]
	v_pk_mul_f32 v[236:237], v[92:93], v[236:237]
	v_pk_mul_f32 v[238:239], v[86:87], v[238:239]
	v_pk_mul_f32 v[240:241], v[88:89], v[240:241]
	v_pk_mul_f32 v[242:243], v[82:83], v[242:243]
	v_pk_mul_f32 v[244:245], v[84:85], v[244:245]
	v_pk_mul_f32 v[78:79], v[78:79], v[230:231]
	v_pk_mul_f32 v[80:81], v[80:81], v[232:233]
	v_pk_mul_f32 v[70:71], v[70:71], v[234:235]
	v_pk_mul_f32 v[72:73], v[72:73], v[236:237]
	v_pk_mul_f32 v[62:63], v[62:63], v[238:239]
	v_pk_mul_f32 v[64:65], v[64:65], v[240:241]
	v_pk_mul_f32 v[54:55], v[54:55], v[242:243]
	v_pk_mul_f32 v[56:57], v[56:57], v[244:245]
	v_med3_f32 v78, v78, s72, v197
	v_med3_f32 v79, v79, s72, v197
	v_med3_f32 v80, v80, s72, v197
	v_med3_f32 v81, v81, s72, v197
	v_med3_f32 v70, v70, s72, v197
	v_med3_f32 v71, v71, s72, v197
	v_med3_f32 v72, v72, s72, v197
	v_med3_f32 v73, v73, s72, v197
	v_med3_f32 v62, v62, s72, v197
	v_med3_f32 v63, v63, s72, v197
	v_med3_f32 v64, v64, s72, v197
	v_med3_f32 v65, v65, s72, v197
	v_med3_f32 v54, v54, s72, v197
	v_med3_f32 v55, v55, s72, v197
	v_med3_f32 v56, v56, s72, v197
	v_med3_f32 v57, v57, s72, v197
	v_cvt_pk_fp8_f32 v246, v78, v79
	v_cvt_pk_fp8_f32 v247, v70, v71
	v_cvt_pk_fp8_f32 v248, v62, v63
	v_cvt_pk_fp8_f32 v249, v54, v55
	v_add_u32_e32 v207, s75, v206
	v_add_u32_e32 v208, s76, v206
	v_cvt_pk_fp8_f32 v246, v80, v81 op_sel:[0,0,1]
	v_cvt_pk_fp8_f32 v247, v72, v73 op_sel:[0,0,1]
	v_cvt_pk_fp8_f32 v248, v64, v65 op_sel:[0,0,1]
	v_cvt_pk_fp8_f32 v249, v56, v57 op_sel:[0,0,1]
	s_nop 1
	global_store_dwordx2 v207, v[246:247], s[100:101]
	global_store_dwordx2 v208, v[248:249], s[100:101]
	v_pk_fma_f32 v[74:75], v[74:75], s[18:19], 0 op_sel_hi:[1,0,0]
	v_pk_fma_f32 v[76:77], v[76:77], s[18:19], 0 op_sel_hi:[1,0,0]
	v_pk_fma_f32 v[66:67], v[66:67], s[18:19], 0 op_sel_hi:[1,0,0]
	v_pk_fma_f32 v[68:69], v[68:69], s[18:19], 0 op_sel_hi:[1,0,0]
	v_pk_fma_f32 v[46:47], v[46:47], s[20:21], 0 op_sel_hi:[1,0,0]
	v_pk_fma_f32 v[48:49], v[48:49], s[20:21], 0 op_sel_hi:[1,0,0]
	v_pk_fma_f32 v[42:43], v[42:43], s[20:21], 0 op_sel_hi:[1,0,0]
	v_pk_fma_f32 v[44:45], v[44:45], s[20:21], 0 op_sel_hi:[1,0,0]
	v_pk_fma_f32 v[58:59], v[58:59], s[18:19], 0 op_sel_hi:[1,0,0]
	v_pk_fma_f32 v[60:61], v[60:61], s[18:19], 0 op_sel_hi:[1,0,0]
	v_pk_fma_f32 v[50:51], v[50:51], s[18:19], 0 op_sel_hi:[1,0,0]
	v_pk_fma_f32 v[52:53], v[52:53], s[18:19], 0 op_sel_hi:[1,0,0]
	v_pk_fma_f32 v[38:39], v[38:39], s[20:21], 0 op_sel_hi:[1,0,0]
	v_pk_fma_f32 v[40:41], v[40:41], s[20:21], 0 op_sel_hi:[1,0,0]
	v_pk_fma_f32 v[34:35], v[34:35], s[20:21], 0 op_sel_hi:[1,0,0]
	v_pk_fma_f32 v[36:37], v[36:37], s[20:21], 0 op_sel_hi:[1,0,0]
	v_pk_mul_f32 v[230:231], v[74:75], s[98:99] op_sel_hi:[1,0]
	v_pk_mul_f32 v[232:233], v[76:77], s[98:99] op_sel_hi:[1,0]
	v_pk_mul_f32 v[234:235], v[66:67], s[98:99] op_sel_hi:[1,0]
	v_pk_mul_f32 v[236:237], v[68:69], s[98:99] op_sel_hi:[1,0]
	v_pk_mul_f32 v[238:239], v[58:59], s[98:99] op_sel_hi:[1,0]
	v_pk_mul_f32 v[240:241], v[60:61], s[98:99] op_sel_hi:[1,0]
	v_pk_mul_f32 v[242:243], v[50:51], s[98:99] op_sel_hi:[1,0]
	v_pk_mul_f32 v[244:245], v[52:53], s[98:99] op_sel_hi:[1,0]
	v_exp_f32_e32 v230, v230
	v_exp_f32_e32 v231, v231
	v_exp_f32_e32 v232, v232
	v_exp_f32_e32 v233, v233
	v_exp_f32_e32 v234, v234
	v_exp_f32_e32 v235, v235
	v_exp_f32_e32 v236, v236
	v_exp_f32_e32 v237, v237
	v_exp_f32_e32 v238, v238
	v_exp_f32_e32 v239, v239
	v_exp_f32_e32 v240, v240
	v_exp_f32_e32 v241, v241
	v_exp_f32_e32 v242, v242
	v_exp_f32_e32 v243, v243
	v_exp_f32_e32 v244, v244
	v_exp_f32_e32 v245, v245
	v_pk_add_f32 v[230:231], v[230:231], 1.0 op_sel_hi:[1,0]
	v_pk_add_f32 v[232:233], v[232:233], 1.0 op_sel_hi:[1,0]
	v_pk_add_f32 v[234:235], v[234:235], 1.0 op_sel_hi:[1,0]
	v_pk_add_f32 v[236:237], v[236:237], 1.0 op_sel_hi:[1,0]
	v_pk_add_f32 v[238:239], v[238:239], 1.0 op_sel_hi:[1,0]
	v_pk_add_f32 v[240:241], v[240:241], 1.0 op_sel_hi:[1,0]
	v_pk_add_f32 v[242:243], v[242:243], 1.0 op_sel_hi:[1,0]
	v_pk_add_f32 v[244:245], v[244:245], 1.0 op_sel_hi:[1,0]
	v_rcp_f32_e32 v230, v230
	v_rcp_f32_e32 v231, v231
	v_rcp_f32_e32 v232, v232
	v_rcp_f32_e32 v233, v233
	v_rcp_f32_e32 v234, v234
	v_rcp_f32_e32 v235, v235
	v_rcp_f32_e32 v236, v236
	v_rcp_f32_e32 v237, v237
	v_rcp_f32_e32 v238, v238
	v_rcp_f32_e32 v239, v239
	v_rcp_f32_e32 v240, v240
	v_rcp_f32_e32 v241, v241
	v_rcp_f32_e32 v242, v242
	v_rcp_f32_e32 v243, v243
	v_rcp_f32_e32 v244, v244
	v_rcp_f32_e32 v245, v245
	v_pk_mul_f32 v[230:231], v[74:75], v[230:231]
	v_pk_mul_f32 v[232:233], v[76:77], v[232:233]
	v_pk_mul_f32 v[234:235], v[66:67], v[234:235]
	v_pk_mul_f32 v[236:237], v[68:69], v[236:237]
	v_pk_mul_f32 v[238:239], v[58:59], v[238:239]
	v_pk_mul_f32 v[240:241], v[60:61], v[240:241]
	v_pk_mul_f32 v[242:243], v[50:51], v[242:243]
	v_pk_mul_f32 v[244:245], v[52:53], v[244:245]
	v_pk_mul_f32 v[46:47], v[46:47], v[230:231]
	v_pk_mul_f32 v[48:49], v[48:49], v[232:233]
	v_pk_mul_f32 v[42:43], v[42:43], v[234:235]
	v_pk_mul_f32 v[44:45], v[44:45], v[236:237]
	v_pk_mul_f32 v[38:39], v[38:39], v[238:239]
	v_pk_mul_f32 v[40:41], v[40:41], v[240:241]
	v_pk_mul_f32 v[34:35], v[34:35], v[242:243]
	v_pk_mul_f32 v[36:37], v[36:37], v[244:245]
	v_med3_f32 v46, v46, s72, v197
	v_med3_f32 v47, v47, s72, v197
	v_med3_f32 v48, v48, s72, v197
	v_med3_f32 v49, v49, s72, v197
	v_med3_f32 v42, v42, s72, v197
	v_med3_f32 v43, v43, s72, v197
	v_med3_f32 v44, v44, s72, v197
	v_med3_f32 v45, v45, s72, v197
	v_med3_f32 v38, v38, s72, v197
	v_med3_f32 v39, v39, s72, v197
	v_med3_f32 v40, v40, s72, v197
	v_med3_f32 v41, v41, s72, v197
	v_med3_f32 v34, v34, s72, v197
	v_med3_f32 v35, v35, s72, v197
	v_med3_f32 v36, v36, s72, v197
	v_med3_f32 v37, v37, s72, v197
	v_cvt_pk_fp8_f32 v250, v46, v47
	v_cvt_pk_fp8_f32 v251, v42, v43
	v_cvt_pk_fp8_f32 v252, v38, v39
	v_cvt_pk_fp8_f32 v253, v34, v35
	v_add_u32_e32 v207, s77, v206
	v_add_u32_e32 v208, 0xf2000, v206
	v_cvt_pk_fp8_f32 v250, v48, v49 op_sel:[0,0,1]
	v_cvt_pk_fp8_f32 v251, v44, v45 op_sel:[0,0,1]
	v_cvt_pk_fp8_f32 v252, v40, v41 op_sel:[0,0,1]
	v_cvt_pk_fp8_f32 v253, v36, v37 op_sel:[0,0,1]
	s_nop 1
	global_store_dwordx2 v207, v[250:251], s[100:101]
	global_store_dwordx2 v208, v[252:253], s[100:101]
	s_mov_b32 s99, 1
	s_andn2_b64 vcc, exec, s[2:3]
	s_mov_b64 s[2:3], -1
	s_cbranch_vccnz .LBB0_2928
	s_andn2_b64 vcc, exec, s[10:11]
	s_cbranch_vccnz .LBB0_2927
	s_barrier
	s_branch .LBB0_2927
